# v13 with v_pk_mul_f32 scaling replaced by plain v_mul_f32 (packed f32 beside MFMA is an anti-lever)
# baseline (speedup 1.0000x reference)
.Lk3m_loop:
	s_waitcnt lgkmcnt(0)
	s_lshl_b32 s84, s70, 13
	s_add_u32 s90, s80, s84
	s_addc_u32 s91, s81, 0
	s_mul_i32 s84, s70, 0xc000
	s_add_u32 s92, s94, s84
	s_addc_u32 s93, s95, 0
	s_add_i32 s84, s70, 2
	s_and_b32 s84, s84, 15
	s_lshl_b32 s82, s84, 12
	s_lshl_b32 s84, s84, 16
	s_add_u32 s84, s84, 0x787000
	s_add_u32 s86, s40, s84
	s_addc_u32 s87, s41, 0
	s_add_u32 s88, s86, 0x1000
	s_addc_u32 s89, s87, 0
	s_add_i32 s84, s70, 15
	s_and_b32 s84, s84, 15
	s_mul_i32 s84, s84, 0xc0
	s_add_u32 s83, s84, 0x10000
	v_add_u32_e32 v112, s82, v105
	v_sub_f32_e32 v120, v94, v114
	v_cmp_eq_f32_e64 s[72:73], v94, v114
	s_waitcnt vmcnt(27)
	v_mfma_f32_16x16x4_f32 v[176:179], v132, v6, 0
	ds_read2st64_b32 v[254:255], v112 offset1:1
	v_sub_f32_e32 v121, v90, v114
	v_cmp_eq_f32_e64 s[74:75], v90, v114
	v_exp_f32_e32 v149, v120
	v_cndmask_b32_e64 v118, v155, 15, s[72:73]
	v_max3_f32 v115, v35, v39, v43
	v_sub_f32_e32 v120, v86, v114
	v_cmp_eq_f32_e64 s[76:77], v86, v114
	v_exp_f32_e32 v148, v121
	v_cndmask_b32_e64 v118, v118, 14, s[74:75]
	v_mfma_f32_16x16x4_f32 v[180:183], v132, v8, 0
	v_sub_f32_e32 v121, v82, v114
	v_max3_f32 v117, v47, v51, v55
	v_cmp_eq_f32_e64 s[72:73], v82, v114
	v_exp_f32_e32 v147, v120
	v_cndmask_b32_e64 v118, v118, 13, s[76:77]
	v_sub_f32_e32 v120, v78, v114
	v_cmp_eq_f32_e64 s[74:75], v78, v114
	v_max3_f32 v115, v115, v59, v63
	v_exp_f32_e32 v146, v121
	v_cndmask_b32_e64 v118, v118, 12, s[72:73]
	v_mfma_f32_16x16x4_f32 v[176:179], v133, v7, v[176:179]
	v_sub_f32_e32 v121, v74, v114
	v_cmp_eq_f32_e64 s[76:77], v74, v114
	v_exp_f32_e32 v145, v120
	v_cndmask_b32_e64 v118, v118, 11, s[74:75]
	v_max3_f32 v117, v117, v67, v71
	v_sub_f32_e32 v120, v70, v114
	v_cmp_eq_f32_e64 s[72:73], v70, v114
	v_exp_f32_e32 v144, v121
	v_cndmask_b32_e64 v118, v118, 10, s[76:77]
	v_mfma_f32_16x16x4_f32 v[180:183], v133, v9, v[180:183]
	global_load_dwordx4 v[6:9], v104, s[86:87]
	v_sub_f32_e32 v121, v66, v114
	v_max3_f32 v115, v115, v75, v79
	v_cmp_eq_f32_e64 s[74:75], v66, v114
	v_exp_f32_e32 v143, v120
	v_cndmask_b32_e64 v118, v118, 9, s[72:73]
	v_sub_f32_e32 v120, v62, v114
	v_cmp_eq_f32_e64 s[76:77], v62, v114
	v_max3_f32 v117, v117, v83, v87
	v_exp_f32_e32 v142, v121
	v_cndmask_b32_e64 v118, v118, 8, s[74:75]
	s_waitcnt vmcnt(27)
	v_mfma_f32_16x16x4_f32 v[184:187], v132, v2, 0
	v_sub_f32_e32 v121, v58, v114
	v_cmp_eq_f32_e64 s[72:73], v58, v114
	v_exp_f32_e32 v141, v120
	v_cndmask_b32_e64 v118, v118, 7, s[76:77]
	v_max3_f32 v115, v115, v91, v95
	v_sub_f32_e32 v120, v54, v114
	v_cmp_eq_f32_e64 s[74:75], v54, v114
	v_exp_f32_e32 v140, v121
	v_cndmask_b32_e64 v118, v118, 6, s[72:73]
	v_mfma_f32_16x16x4_f32 v[188:191], v132, v4, 0
	v_sub_f32_e32 v121, v50, v114
	v_max_f32_e32 v115, v115, v117
	v_cmp_eq_f32_e64 s[76:77], v50, v114
	v_exp_f32_e32 v139, v120
	v_cndmask_b32_e64 v118, v118, 5, s[74:75]
	v_sub_f32_e32 v120, v46, v114
	v_cmp_eq_f32_e64 s[72:73], v46, v114
	v_max_f32_dpp v115, v115, v115 row_ror:1 row_mask:0xf bank_mask:0xf
	v_exp_f32_e32 v138, v121
	v_cndmask_b32_e64 v118, v118, 4, s[76:77]
	v_mfma_f32_16x16x4_f32 v[184:187], v133, v3, v[184:187]
	v_sub_f32_e32 v121, v42, v114
	v_cmp_eq_f32_e64 s[74:75], v42, v114
	v_exp_f32_e32 v137, v120
	v_cndmask_b32_e64 v118, v118, 3, s[72:73]
	v_max_f32_dpp v115, v115, v115 row_ror:2 row_mask:0xf bank_mask:0xf
	v_sub_f32_e32 v120, v38, v114
	v_cmp_eq_f32_e64 s[76:77], v38, v114
	v_exp_f32_e32 v136, v121
	v_cndmask_b32_e64 v118, v118, 2, s[74:75]
	v_mfma_f32_16x16x4_f32 v[188:191], v133, v5, v[188:191]
	global_load_dwordx4 v[2:5], v104, s[86:87] offset:1024
	v_sub_f32_e32 v121, v34, v114
	v_max_f32_dpp v115, v115, v115 row_ror:4 row_mask:0xf bank_mask:0xf
	v_cmp_eq_f32_e64 s[72:73], v34, v114
	v_exp_f32_e32 v135, v120
	v_cndmask_b32_e64 v118, v118, 1, s[76:77]
	v_exp_f32_e32 v134, v121
	v_cndmask_b32_e64 v118, v118, 0, s[72:73]
	v_max_f32_dpp v115, v115, v115 row_ror:8 row_mask:0xf bank_mask:0xf
	v_sub_f32_e32 v120, v95, v115
	v_cmp_eq_f32_e64 s[72:73], v95, v115
	v_max3_f32 v114, v36, v40, v44
	s_waitcnt vmcnt(27)
	v_mfma_f32_16x16x4_f32 v[192:195], v132, v10, 0
	v_sub_f32_e32 v121, v91, v115
	v_and_b32_e32 v122, 12, v118
	v_cmp_eq_f32_e64 s[74:75], v91, v115
	v_and_b32_e32 v124, 3, v118
	v_exp_f32_e32 v175, v120
	v_add_f32_e32 v128, v134, v135
	v_cndmask_b32_e64 v119, v155, 15, s[72:73]
	v_add_f32_e32 v130, v136, v137
	v_sub_f32_e32 v120, v87, v115
	v_lshl_or_b32 v122, v122, 4, v124
	v_cmp_eq_f32_e64 s[76:77], v87, v115
	v_max3_f32 v116, v48, v52, v56
	v_exp_f32_e32 v174, v121
	v_add_f32_e32 v128, v128, v138
	v_cndmask_b32_e64 v119, v119, 14, s[74:75]
	v_add_f32_e32 v130, v130, v139
	v_mfma_f32_16x16x4_f32 v[196:199], v132, v12, 0
	v_sub_f32_e32 v121, v83, v115
	v_or_b32_e32 v122, v122, v102
	v_cmp_eq_f32_e64 s[72:73], v83, v115
	v_add_f32_e32 v128, v128, v140
	v_exp_f32_e32 v173, v120
	v_max3_f32 v114, v114, v60, v64
	v_cndmask_b32_e64 v119, v119, 13, s[76:77]
	v_add_f32_e32 v130, v130, v141
	v_sub_f32_e32 v120, v79, v115
	v_max_u32_e32 v126, v122, v118
	v_cmp_eq_f32_e64 s[74:75], v79, v115
	v_add_f32_e32 v128, v128, v142
	v_exp_f32_e32 v172, v121
	v_add_f32_e32 v130, v130, v143
	v_cndmask_b32_e64 v119, v119, 12, s[72:73]
	v_max3_f32 v116, v116, v68, v72
	v_mfma_f32_16x16x4_f32 v[192:195], v133, v11, v[192:195]
	v_sub_f32_e32 v121, v75, v115
	v_min_u32_dpp v126, v126, v126 row_ror:1 row_mask:0xf bank_mask:0xf
	v_cmp_eq_f32_e64 s[76:77], v75, v115
	v_add_f32_e32 v128, v128, v144
	v_exp_f32_e32 v171, v120
	v_add_f32_e32 v130, v130, v145
	v_cndmask_b32_e64 v119, v119, 11, s[74:75]
	v_min_u32_dpp v126, v126, v126 row_ror:2 row_mask:0xf bank_mask:0xf
	v_sub_f32_e32 v120, v71, v115
	v_max3_f32 v114, v114, v76, v80
	v_cmp_eq_f32_e64 s[72:73], v71, v115
	v_add_f32_e32 v128, v128, v146
	v_exp_f32_e32 v170, v121
	v_add_f32_e32 v130, v130, v147
	v_cndmask_b32_e64 v119, v119, 10, s[76:77]
	v_min_u32_dpp v126, v126, v126 row_ror:4 row_mask:0xf bank_mask:0xf
	v_mfma_f32_16x16x4_f32 v[196:199], v133, v13, v[196:199]
	global_load_dwordx4 v[10:13], v104, s[86:87] offset:2048
	v_sub_f32_e32 v121, v67, v115
	v_add_f32_e32 v128, v128, v148
	v_cmp_eq_f32_e64 s[74:75], v67, v115
	v_add_f32_e32 v130, v130, v149
	v_exp_f32_e32 v169, v120
	v_max3_f32 v116, v116, v84, v88
	v_cndmask_b32_e64 v119, v119, 9, s[72:73]
	v_min_u32_dpp v126, v126, v126 row_ror:8 row_mask:0xf bank_mask:0xf
	v_sub_f32_e32 v120, v63, v115
	v_add_f32_e32 v128, v128, v130
	v_cmp_eq_f32_e64 s[76:77], v63, v115
	v_mad_u32_u24 v248, v126, 24, v107
	v_exp_f32_e32 v168, v121
	v_add_f32_dpp v128, v128, v128 row_ror:1 row_mask:0xf bank_mask:0xf
	v_cndmask_b32_e64 v119, v119, 8, s[74:75]
	v_max3_f32 v114, v114, v92, v96
	s_waitcnt vmcnt(23)
	v_mfma_f32_16x16x4_f32 v[200:203], v132, v14, 0
	v_sub_f32_e32 v121, v59, v115
	global_load_dword v240, v248, s[92:93]
	v_cmp_eq_f32_e64 s[72:73], v59, v115
	v_add_f32_dpp v128, v128, v128 row_ror:2 row_mask:0xf bank_mask:0xf
	v_exp_f32_e32 v167, v120
	s_nop 0
	v_add_f32_dpp v128, v128, v128 row_ror:4 row_mask:0xf bank_mask:0xf
	v_cndmask_b32_e64 v119, v119, 7, s[76:77]
	s_nop 0
	v_add_f32_dpp v128, v128, v128 row_ror:8 row_mask:0xf bank_mask:0xf
	v_sub_f32_e32 v120, v55, v115
	v_max_f32_e32 v114, v114, v116
	v_cmp_eq_f32_e64 s[74:75], v55, v115
	v_rcp_f32_e32 v244, v128
	v_exp_f32_e32 v166, v121
	v_mul_f32_e32 v134, v244, v134
	v_cndmask_b32_e64 v119, v119, 6, s[72:73]
	v_mul_f32_e32 v135, v244, v135
	v_mfma_f32_16x16x4_f32 v[204:207], v132, v16, 0
	v_sub_f32_e32 v121, v51, v115
	v_mul_f32_e32 v136, v244, v136
	v_cmp_eq_f32_e64 s[76:77], v51, v115
	v_max_f32_dpp v114, v114, v114 row_ror:1 row_mask:0xf bank_mask:0xf
	v_exp_f32_e32 v165, v120
	v_mul_f32_e32 v137, v244, v137
	v_cndmask_b32_e64 v119, v119, 5, s[74:75]
	global_store_dwordx4 v108, v[134:137], s[90:91] sc1
	v_sub_f32_e32 v120, v47, v115
	v_mul_f32_e32 v138, v244, v138
	v_cmp_eq_f32_e64 s[72:73], v47, v115
	v_mul_f32_e32 v139, v244, v139
	v_exp_f32_e32 v164, v121
	v_mul_f32_e32 v140, v244, v140
	v_cndmask_b32_e64 v119, v119, 4, s[76:77]
	v_max_f32_dpp v114, v114, v114 row_ror:2 row_mask:0xf bank_mask:0xf
	v_mfma_f32_16x16x4_f32 v[200:203], v133, v15, v[200:203]
	v_sub_f32_e32 v121, v43, v115
	v_mul_f32_e32 v141, v244, v141
	v_cmp_eq_f32_e64 s[74:75], v43, v115
	global_store_dwordx4 v108, v[138:141], s[90:91] offset:256 sc1
	v_exp_f32_e32 v163, v120
	v_mul_f32_e32 v142, v244, v142
	v_cndmask_b32_e64 v119, v119, 3, s[72:73]
	v_mul_f32_e32 v143, v244, v143
	v_sub_f32_e32 v120, v39, v115
	v_max_f32_dpp v114, v114, v114 row_ror:4 row_mask:0xf bank_mask:0xf
	v_cmp_eq_f32_e64 s[76:77], v39, v115
	v_mul_f32_e32 v144, v244, v144
	v_exp_f32_e32 v162, v121
	v_mul_f32_e32 v145, v244, v145
	v_cndmask_b32_e64 v119, v119, 2, s[74:75]
	global_store_dwordx4 v108, v[142:145], s[90:91] offset:512 sc1
	v_mfma_f32_16x16x4_f32 v[204:207], v133, v17, v[204:207]
	global_load_dwordx4 v[14:17], v104, s[86:87] offset:3072
	v_sub_f32_e32 v121, v35, v115
	v_mul_f32_e32 v146, v244, v146
	v_cmp_eq_f32_e64 s[72:73], v35, v115
	v_max_f32_dpp v114, v114, v114 row_ror:8 row_mask:0xf bank_mask:0xf
	v_exp_f32_e32 v161, v120
	v_mul_f32_e32 v147, v244, v147
	v_cndmask_b32_e64 v119, v119, 1, s[76:77]
	v_mul_f32_e32 v148, v244, v148
	v_exp_f32_e32 v160, v121
	v_mul_f32_e32 v149, v244, v149
	v_cndmask_b32_e64 v119, v119, 0, s[72:73]
	global_store_dwordx4 v108, v[146:149], s[90:91] offset:768 sc1
	v_sub_f32_e32 v120, v96, v114
	s_waitcnt vmcnt(13)
	v_cmp_eq_f32_e64 s[72:73], v96, v114
	v_add_u32_e32 v113, s83, v106
	s_waitcnt vmcnt(27)
	v_mfma_f32_16x16x4_f32 v[208:211], v132, v18, 0
	v_sub_f32_e32 v121, v92, v114
	ds_read2st64_b32 v[250:251], v113 offset1:12
	v_cmp_eq_f32_e64 s[74:75], v92, v114
	ds_read2st64_b32 v[252:253], v113 offset0:24 offset1:36
	v_exp_f32_e32 v149, v120
	v_max3_f32 v115, v37, v41, v45
	v_cndmask_b32_e64 v118, v155, 15, s[72:73]
	v_and_b32_e32 v123, 12, v119
	v_sub_f32_e32 v120, v88, v114
	v_and_b32_e32 v125, 3, v119
	v_cmp_eq_f32_e64 s[76:77], v88, v114
	v_add_f32_e32 v129, v160, v161
	v_exp_f32_e32 v148, v121
	v_add_f32_e32 v131, v162, v163
	v_cndmask_b32_e64 v118, v118, 14, s[74:75]
	v_lshl_or_b32 v123, v123, 4, v125
	v_mfma_f32_16x16x4_f32 v[212:215], v132, v20, 0
	v_sub_f32_e32 v121, v84, v114
	v_max3_f32 v117, v49, v53, v57
	v_cmp_eq_f32_e64 s[72:73], v84, v114
	v_add_f32_e32 v129, v129, v164
	v_exp_f32_e32 v147, v120
	v_add_f32_e32 v131, v131, v165
	v_cndmask_b32_e64 v118, v118, 13, s[76:77]
	v_or_b32_e32 v123, v123, v102
	v_sub_f32_e32 v120, v80, v114
	v_add_f32_e32 v129, v129, v166
	v_cmp_eq_f32_e64 s[74:75], v80, v114
	v_max3_f32 v115, v115, v61, v65
	v_exp_f32_e32 v146, v121
	v_add_f32_e32 v131, v131, v167
	v_cndmask_b32_e64 v118, v118, 12, s[72:73]
	v_max_u32_e32 v127, v123, v119
	v_mfma_f32_16x16x4_f32 v[208:211], v133, v19, v[208:211]
	v_sub_f32_e32 v121, v76, v114
	v_add_f32_e32 v129, v129, v168
	v_cmp_eq_f32_e64 s[76:77], v76, v114
	v_add_f32_e32 v131, v131, v169
	v_exp_f32_e32 v145, v120
	v_max3_f32 v117, v117, v69, v73
	v_cndmask_b32_e64 v118, v118, 11, s[74:75]
	v_min_u32_dpp v127, v127, v127 row_ror:1 row_mask:0xf bank_mask:0xf
	v_add_f32_e32 v129, v129, v170
	v_sub_f32_e32 v120, v72, v114
	v_add_f32_e32 v131, v131, v171
	v_cmp_eq_f32_e64 s[72:73], v72, v114
	v_min_u32_dpp v127, v127, v127 row_ror:2 row_mask:0xf bank_mask:0xf
	v_exp_f32_e32 v144, v121
	v_max3_f32 v115, v115, v77, v81
	v_cndmask_b32_e64 v118, v118, 10, s[76:77]
	v_add_f32_e32 v129, v129, v172
	v_mfma_f32_16x16x4_f32 v[212:215], v133, v21, v[212:215]
	global_load_dwordx4 v[18:21], v104, s[88:89]
	v_sub_f32_e32 v121, v68, v114
	v_add_f32_e32 v131, v131, v173
	v_cmp_eq_f32_e64 s[74:75], v68, v114
	v_min_u32_dpp v127, v127, v127 row_ror:4 row_mask:0xf bank_mask:0xf
	v_exp_f32_e32 v143, v120
	v_add_f32_e32 v129, v129, v174
	v_cndmask_b32_e64 v118, v118, 9, s[72:73]
	v_add_f32_e32 v131, v131, v175
	v_sub_f32_e32 v120, v64, v114
	v_max3_f32 v117, v117, v85, v89
	v_cmp_eq_f32_e64 s[76:77], v64, v114
	v_min_u32_dpp v127, v127, v127 row_ror:8 row_mask:0xf bank_mask:0xf
	v_exp_f32_e32 v142, v121
	v_add_f32_e32 v129, v129, v131
	v_cndmask_b32_e64 v118, v118, 8, s[74:75]
	v_mad_u32_u24 v249, v127, 24, v107
	s_waitcnt vmcnt(24)
	v_mfma_f32_16x16x4_f32 v[216:219], v132, v22, 0
	v_sub_f32_e32 v121, v60, v114
	v_add_f32_dpp v129, v129, v129 row_ror:1 row_mask:0xf bank_mask:0xf
	v_cmp_eq_f32_e64 s[72:73], v60, v114
	v_max3_f32 v115, v115, v93, v97
	v_exp_f32_e32 v141, v120
	global_load_dword v241, v249, s[92:93]
	v_cndmask_b32_e64 v118, v118, 7, s[76:77]
	v_add_f32_dpp v129, v129, v129 row_ror:2 row_mask:0xf bank_mask:0xf
	v_sub_f32_e32 v120, v56, v114
	s_nop 0
	v_add_f32_dpp v129, v129, v129 row_ror:4 row_mask:0xf bank_mask:0xf
	v_cmp_eq_f32_e64 s[74:75], v56, v114
	s_nop 0
	v_add_f32_dpp v129, v129, v129 row_ror:8 row_mask:0xf bank_mask:0xf
	v_exp_f32_e32 v140, v121
	v_max_f32_e32 v115, v115, v117
	v_cndmask_b32_e64 v118, v118, 6, s[72:73]
	v_rcp_f32_e32 v246, v129
	v_mfma_f32_16x16x4_f32 v[220:223], v132, v24, 0
	v_sub_f32_e32 v121, v52, v114
	v_mul_f32_e32 v160, v246, v160
	v_mul_f32_e32 v161, v246, v161
	v_cmp_eq_f32_e64 s[76:77], v52, v114
	v_mul_f32_e32 v162, v246, v162
	v_exp_f32_e32 v139, v120
	v_max_f32_dpp v115, v115, v115 row_ror:1 row_mask:0xf bank_mask:0xf
	v_cndmask_b32_e64 v118, v118, 5, s[74:75]
	v_mul_f32_e32 v163, v246, v163
	v_sub_f32_e32 v120, v48, v114
	global_store_dwordx4 v109, v[160:163], s[90:91] sc1
	v_cmp_eq_f32_e64 s[72:73], v48, v114
	v_mul_f32_e32 v164, v246, v164
	v_exp_f32_e32 v138, v121
	v_mul_f32_e32 v165, v246, v165
	v_cndmask_b32_e64 v118, v118, 4, s[76:77]
	v_mul_f32_e32 v166, v246, v166
	v_mfma_f32_16x16x4_f32 v[216:219], v133, v23, v[216:219]
	v_sub_f32_e32 v121, v44, v114
	v_max_f32_dpp v115, v115, v115 row_ror:2 row_mask:0xf bank_mask:0xf
	v_cmp_eq_f32_e64 s[74:75], v44, v114
	v_mul_f32_e32 v167, v246, v167
	v_exp_f32_e32 v137, v120
	global_store_dwordx4 v109, v[164:167], s[90:91] offset:256 sc1
	v_cndmask_b32_e64 v118, v118, 3, s[72:73]
	v_mul_f32_e32 v168, v246, v168
	v_sub_f32_e32 v120, v40, v114
	v_mul_f32_e32 v169, v246, v169
	v_cmp_eq_f32_e64 s[76:77], v40, v114
	v_max_f32_dpp v115, v115, v115 row_ror:4 row_mask:0xf bank_mask:0xf
	v_exp_f32_e32 v136, v121
	v_mul_f32_e32 v170, v246, v170
	v_cndmask_b32_e64 v118, v118, 2, s[74:75]
	v_mul_f32_e32 v171, v246, v171
	v_mfma_f32_16x16x4_f32 v[220:223], v133, v25, v[220:223]
	global_load_dwordx4 v[22:25], v104, s[88:89] offset:1024
	v_sub_f32_e32 v121, v36, v114
	global_store_dwordx4 v109, v[168:171], s[90:91] offset:512 sc1
	v_cmp_eq_f32_e64 s[72:73], v36, v114
	v_mul_f32_e32 v172, v246, v172
	v_exp_f32_e32 v135, v120
	v_max_f32_dpp v115, v115, v115 row_ror:8 row_mask:0xf bank_mask:0xf
	v_cndmask_b32_e64 v118, v118, 1, s[76:77]
	v_mul_f32_e32 v173, v246, v173
	v_exp_f32_e32 v134, v121
	v_mul_f32_e32 v174, v246, v174
	v_cndmask_b32_e64 v118, v118, 0, s[72:73]
	v_mul_f32_e32 v175, v246, v175
	global_store_dwordx4 v109, v[172:175], s[90:91] offset:768 sc1
	v_sub_f32_e32 v120, v97, v115
	v_cmp_eq_f32_e64 s[72:73], v97, v115
	s_waitcnt lgkmcnt(0)
	s_waitcnt vmcnt(27)
	v_mfma_f32_16x16x4_f32 v[224:227], v132, v26, 0
	v_sub_f32_e32 v121, v93, v115
	v_add_f32_e32 v250, v159, v250
	v_cmp_eq_f32_e64 s[74:75], v93, v115
	v_add_f32_e32 v251, v158, v251
	v_exp_f32_e32 v175, v120
	v_add_f32_e32 v252, v157, v252
	v_cndmask_b32_e64 v119, v155, 15, s[72:73]
	v_add_f32_e32 v253, v156, v253
	v_sub_f32_e32 v120, v89, v115
	ds_write2st64_b32 v113, v250, v251 offset1:12
	v_cmp_eq_f32_e64 s[76:77], v89, v115
	ds_write2st64_b32 v113, v252, v253 offset0:24 offset1:36
	v_exp_f32_e32 v174, v121
	v_and_b32_e32 v122, 12, v118
	v_cndmask_b32_e64 v119, v119, 14, s[74:75]
	v_and_b32_e32 v124, 3, v118
	v_mfma_f32_16x16x4_f32 v[228:231], v132, v28, 0
	v_sub_f32_e32 v121, v85, v115
	v_cmp_eq_f32_e64 s[72:73], v85, v115
	v_add_f32_e32 v128, v134, v135
	v_exp_f32_e32 v173, v120
	v_add_f32_e32 v130, v136, v137
	v_cndmask_b32_e64 v119, v119, 13, s[76:77]
	v_lshl_or_b32 v122, v122, 4, v124
	v_sub_f32_e32 v120, v81, v115
	v_add_f32_e32 v128, v128, v138
	v_cmp_eq_f32_e64 s[74:75], v81, v115
	v_add_f32_e32 v130, v130, v139
	v_exp_f32_e32 v172, v121
	v_or_b32_e32 v122, v122, v102
	v_cndmask_b32_e64 v119, v119, 12, s[72:73]
	v_add_f32_e32 v128, v128, v140
	v_mfma_f32_16x16x4_f32 v[224:227], v133, v27, v[224:227]
	v_sub_f32_e32 v121, v77, v115
	v_add_f32_e32 v130, v130, v141
	v_cmp_eq_f32_e64 s[76:77], v77, v115
	v_max_u32_e32 v126, v122, v118
	v_exp_f32_e32 v171, v120
	v_add_f32_e32 v128, v128, v142
	v_cndmask_b32_e64 v119, v119, 11, s[74:75]
	v_sub_f32_e32 v120, v73, v115
	v_add_f32_e32 v130, v130, v143
	v_cmp_eq_f32_e64 s[72:73], v73, v115
	v_min_u32_dpp v126, v126, v126 row_ror:1 row_mask:0xf bank_mask:0xf
	v_exp_f32_e32 v170, v121
	v_add_f32_e32 v128, v128, v144
	v_cndmask_b32_e64 v119, v119, 10, s[76:77]
	v_add_f32_e32 v130, v130, v145
	v_mfma_f32_16x16x4_f32 v[228:231], v133, v29, v[228:231]
	global_load_dwordx4 v[26:29], v104, s[88:89] offset:2048
	v_sub_f32_e32 v121, v69, v115
	v_min_u32_dpp v126, v126, v126 row_ror:2 row_mask:0xf bank_mask:0xf
	v_cmp_eq_f32_e64 s[74:75], v69, v115
	v_add_f32_e32 v128, v128, v146
	v_exp_f32_e32 v169, v120
	v_add_f32_e32 v130, v130, v147
	v_cndmask_b32_e64 v119, v119, 9, s[72:73]
	v_min_u32_dpp v126, v126, v126 row_ror:4 row_mask:0xf bank_mask:0xf
	v_sub_f32_e32 v120, v65, v115
	v_add_f32_e32 v128, v128, v148
	v_cmp_eq_f32_e64 s[76:77], v65, v115
	v_add_f32_e32 v130, v130, v149
	v_exp_f32_e32 v168, v121
	v_cndmask_b32_e64 v119, v119, 8, s[74:75]
	v_min_u32_dpp v126, v126, v126 row_ror:8 row_mask:0xf bank_mask:0xf
	s_waitcnt vmcnt(24)
	v_mfma_f32_16x16x4_f32 v[232:235], v132, v30, 0
	v_sub_f32_e32 v121, v61, v115
	v_add_f32_e32 v128, v128, v130
	v_cmp_eq_f32_e64 s[72:73], v61, v115
	v_mad_u32_u24 v248, v126, 24, v107
	v_exp_f32_e32 v167, v120
	v_add_f32_dpp v128, v128, v128 row_ror:1 row_mask:0xf bank_mask:0xf
	v_cndmask_b32_e64 v119, v119, 7, s[76:77]
	global_load_dword v242, v248, s[92:93]
	v_sub_f32_e32 v120, v57, v115
	v_add_f32_dpp v128, v128, v128 row_ror:2 row_mask:0xf bank_mask:0xf
	v_cmp_eq_f32_e64 s[74:75], v57, v115
	s_nop 0
	v_add_f32_dpp v128, v128, v128 row_ror:4 row_mask:0xf bank_mask:0xf
	v_exp_f32_e32 v166, v121
	s_nop 0
	v_add_f32_dpp v128, v128, v128 row_ror:8 row_mask:0xf bank_mask:0xf
	v_cndmask_b32_e64 v119, v119, 6, s[72:73]
	v_rcp_f32_e32 v244, v128
	v_mfma_f32_16x16x4_f32 v[236:239], v132, v32, 0
	v_sub_f32_e32 v121, v53, v115
	v_cmp_eq_f32_e64 s[76:77], v53, v115
	v_mul_f32_e32 v134, v244, v134
	v_exp_f32_e32 v165, v120
	v_mul_f32_e32 v135, v244, v135
	v_cndmask_b32_e64 v119, v119, 5, s[74:75]
	v_mul_f32_e32 v136, v244, v136
	v_sub_f32_e32 v120, v49, v115
	v_mul_f32_e32 v137, v244, v137
	v_cmp_eq_f32_e64 s[72:73], v49, v115
	global_store_dwordx4 v110, v[134:137], s[90:91] sc1
	v_exp_f32_e32 v164, v121
	v_mul_f32_e32 v138, v244, v138
	v_cndmask_b32_e64 v119, v119, 4, s[76:77]
	v_mul_f32_e32 v139, v244, v139
	v_mfma_f32_16x16x4_f32 v[232:235], v133, v31, v[232:235]
	v_sub_f32_e32 v121, v45, v115
	v_mul_f32_e32 v140, v244, v140
	v_cmp_eq_f32_e64 s[74:75], v45, v115
	v_mul_f32_e32 v141, v244, v141
	v_exp_f32_e32 v163, v120
	global_store_dwordx4 v110, v[138:141], s[90:91] offset:256 sc1
	v_cndmask_b32_e64 v119, v119, 3, s[72:73]
	v_sub_f32_e32 v120, v41, v115
	v_mul_f32_e32 v142, v244, v142
	v_cmp_eq_f32_e64 s[76:77], v41, v115
	v_mul_f32_e32 v143, v244, v143
	v_exp_f32_e32 v162, v121
	v_mul_f32_e32 v144, v244, v144
	v_cndmask_b32_e64 v119, v119, 2, s[74:75]
	v_mul_f32_e32 v145, v244, v145
	v_mfma_f32_16x16x4_f32 v[236:239], v133, v33, v[236:239]
	global_load_dwordx4 v[30:33], v104, s[88:89] offset:3072
	v_sub_f32_e32 v121, v37, v115
	global_store_dwordx4 v110, v[142:145], s[90:91] offset:512 sc1
	v_cmp_eq_f32_e64 s[72:73], v37, v115
	v_mul_f32_e32 v146, v244, v146
	v_exp_f32_e32 v161, v120
	v_mul_f32_e32 v147, v244, v147
	v_cndmask_b32_e64 v119, v119, 1, s[76:77]
	v_mul_f32_e32 v148, v244, v148
	v_exp_f32_e32 v160, v121
	v_mul_f32_e32 v149, v244, v149
	v_cndmask_b32_e64 v119, v119, 0, s[72:73]
	global_store_dwordx4 v110, v[146:149], s[90:91] offset:768 sc1
	v_and_b32_e32 v123, 12, v119
	v_max3_f32 v114, v176, v180, v184
	v_and_b32_e32 v125, 3, v119
	v_add_f32_e32 v129, v160, v161
	v_add_f32_e32 v131, v162, v163
	v_lshl_or_b32 v123, v123, 4, v125
	v_max3_f32 v116, v188, v192, v196
	v_add_f32_e32 v129, v129, v164
	v_add_f32_e32 v131, v131, v165
	v_or_b32_e32 v123, v123, v102
	v_add_f32_e32 v129, v129, v166
	v_max3_f32 v114, v114, v200, v204
	v_add_f32_e32 v131, v131, v167
	v_max_u32_e32 v127, v123, v119
	v_add_f32_e32 v129, v129, v168
	v_add_f32_e32 v131, v131, v169
	v_max3_f32 v116, v116, v208, v212
	v_min_u32_dpp v127, v127, v127 row_ror:1 row_mask:0xf bank_mask:0xf
	v_add_f32_e32 v129, v129, v170
	v_add_f32_e32 v131, v131, v171
	v_min_u32_dpp v127, v127, v127 row_ror:2 row_mask:0xf bank_mask:0xf
	v_add_f32_e32 v129, v129, v172
	v_max3_f32 v114, v114, v216, v220
	v_add_f32_e32 v131, v131, v173
	v_min_u32_dpp v127, v127, v127 row_ror:4 row_mask:0xf bank_mask:0xf
	v_add_f32_e32 v129, v129, v174
	v_add_f32_e32 v131, v131, v175
	v_max3_f32 v116, v116, v224, v228
	v_min_u32_dpp v127, v127, v127 row_ror:8 row_mask:0xf bank_mask:0xf
	v_add_f32_e32 v129, v129, v131
	v_mad_u32_u24 v249, v127, 24, v107
	s_nop 0
	v_add_f32_dpp v129, v129, v129 row_ror:1 row_mask:0xf bank_mask:0xf
	v_max3_f32 v114, v114, v232, v236
	global_load_dword v243, v249, s[92:93]
	v_add_f32_dpp v129, v129, v129 row_ror:2 row_mask:0xf bank_mask:0xf
	s_nop 1
	v_add_f32_dpp v129, v129, v129 row_ror:4 row_mask:0xf bank_mask:0xf
	s_nop 1
	v_add_f32_dpp v129, v129, v129 row_ror:8 row_mask:0xf bank_mask:0xf
	v_max_f32_e32 v114, v114, v116
	v_rcp_f32_e32 v246, v129
	s_nop 0
	v_mul_f32_e32 v160, v246, v160
	v_mul_f32_e32 v161, v246, v161
	v_mul_f32_e32 v162, v246, v162
	v_mul_f32_e32 v163, v246, v163
	v_max_f32_dpp v114, v114, v114 row_ror:1 row_mask:0xf bank_mask:0xf
	global_store_dwordx4 v111, v[160:163], s[90:91] sc1
	v_mul_f32_e32 v164, v246, v164
	v_mul_f32_e32 v165, v246, v165
	v_mul_f32_e32 v166, v246, v166
	v_max_f32_dpp v114, v114, v114 row_ror:2 row_mask:0xf bank_mask:0xf
	v_mul_f32_e32 v167, v246, v167
	global_store_dwordx4 v111, v[164:167], s[90:91] offset:256 sc1
	v_mul_f32_e32 v168, v246, v168
	v_mul_f32_e32 v169, v246, v169
	v_max_f32_dpp v114, v114, v114 row_ror:4 row_mask:0xf bank_mask:0xf
	v_mul_f32_e32 v170, v246, v170
	v_mul_f32_e32 v171, v246, v171
	global_store_dwordx4 v111, v[168:171], s[90:91] offset:512 sc1
	v_mul_f32_e32 v172, v246, v172
	v_max_f32_dpp v114, v114, v114 row_ror:8 row_mask:0xf bank_mask:0xf
	v_mul_f32_e32 v173, v246, v173
	v_mul_f32_e32 v174, v246, v174
	v_mul_f32_e32 v175, v246, v175
	global_store_dwordx4 v111, v[172:175], s[90:91] offset:768 sc1
	s_add_i32 s70, s70, 1
	s_waitcnt lgkmcnt(0)
	s_lshl_b32 s84, s70, 13
	s_add_u32 s90, s80, s84
	s_addc_u32 s91, s81, 0
	s_mul_i32 s84, s70, 0xc000
	s_add_u32 s92, s94, s84
	s_addc_u32 s93, s95, 0
	s_add_i32 s84, s70, 2
	s_and_b32 s84, s84, 15
	s_lshl_b32 s82, s84, 12
	s_lshl_b32 s84, s84, 16
	s_add_u32 s84, s84, 0x787000
	s_add_u32 s86, s40, s84
	s_addc_u32 s87, s41, 0
	s_add_u32 s88, s86, 0x1000
	s_addc_u32 s89, s87, 0
	s_add_i32 s84, s70, 15
	s_and_b32 s84, s84, 15
	s_mul_i32 s84, s84, 0xc0
	s_add_u32 s83, s84, 0x10000
	v_add_u32_e32 v112, s82, v105
	v_sub_f32_e32 v120, v236, v114
	v_cmp_eq_f32_e64 s[72:73], v236, v114
	s_waitcnt vmcnt(27)
	v_mfma_f32_16x16x4_f32 v[34:37], v254, v6, 0
	ds_read2st64_b32 v[132:133], v112 offset1:1
	v_sub_f32_e32 v121, v232, v114
	v_cmp_eq_f32_e64 s[74:75], v232, v114
	v_exp_f32_e32 v149, v120
	v_cndmask_b32_e64 v118, v155, 15, s[72:73]
	v_max3_f32 v115, v177, v181, v185
	v_sub_f32_e32 v120, v228, v114
	v_cmp_eq_f32_e64 s[76:77], v228, v114
	v_exp_f32_e32 v148, v121
	v_cndmask_b32_e64 v118, v118, 14, s[74:75]
	v_mfma_f32_16x16x4_f32 v[38:41], v254, v8, 0
	v_sub_f32_e32 v121, v224, v114
	v_max3_f32 v117, v189, v193, v197
	v_cmp_eq_f32_e64 s[72:73], v224, v114
	v_exp_f32_e32 v147, v120
	v_cndmask_b32_e64 v118, v118, 13, s[76:77]
	v_sub_f32_e32 v120, v220, v114
	v_cmp_eq_f32_e64 s[74:75], v220, v114
	v_max3_f32 v115, v115, v201, v205
	v_exp_f32_e32 v146, v121
	v_cndmask_b32_e64 v118, v118, 12, s[72:73]
	v_mfma_f32_16x16x4_f32 v[34:37], v255, v7, v[34:37]
	v_sub_f32_e32 v121, v216, v114
	v_cmp_eq_f32_e64 s[76:77], v216, v114
	v_exp_f32_e32 v145, v120
	v_cndmask_b32_e64 v118, v118, 11, s[74:75]
	v_max3_f32 v117, v117, v209, v213
	v_sub_f32_e32 v120, v212, v114
	v_cmp_eq_f32_e64 s[72:73], v212, v114
	v_exp_f32_e32 v144, v121
	v_cndmask_b32_e64 v118, v118, 10, s[76:77]
	v_mfma_f32_16x16x4_f32 v[38:41], v255, v9, v[38:41]
	global_load_dwordx4 v[6:9], v104, s[86:87]
	v_sub_f32_e32 v121, v208, v114
	v_max3_f32 v115, v115, v217, v221
	v_cmp_eq_f32_e64 s[74:75], v208, v114
	v_exp_f32_e32 v143, v120
	v_cndmask_b32_e64 v118, v118, 9, s[72:73]
	v_sub_f32_e32 v120, v204, v114
	v_cmp_eq_f32_e64 s[76:77], v204, v114
	v_max3_f32 v117, v117, v225, v229
	v_exp_f32_e32 v142, v121
	v_cndmask_b32_e64 v118, v118, 8, s[74:75]
	s_waitcnt vmcnt(27)
	v_mfma_f32_16x16x4_f32 v[42:45], v254, v2, 0
	v_sub_f32_e32 v121, v200, v114
	v_cmp_eq_f32_e64 s[72:73], v200, v114
	v_exp_f32_e32 v141, v120
	v_cndmask_b32_e64 v118, v118, 7, s[76:77]
	v_max3_f32 v115, v115, v233, v237
	v_sub_f32_e32 v120, v196, v114
	v_cmp_eq_f32_e64 s[74:75], v196, v114
	v_exp_f32_e32 v140, v121
	v_cndmask_b32_e64 v118, v118, 6, s[72:73]
	v_mfma_f32_16x16x4_f32 v[46:49], v254, v4, 0
	v_sub_f32_e32 v121, v192, v114
	v_max_f32_e32 v115, v115, v117
	v_cmp_eq_f32_e64 s[76:77], v192, v114
	v_exp_f32_e32 v139, v120
	v_cndmask_b32_e64 v118, v118, 5, s[74:75]
	v_sub_f32_e32 v120, v188, v114
	v_cmp_eq_f32_e64 s[72:73], v188, v114
	v_max_f32_dpp v115, v115, v115 row_ror:1 row_mask:0xf bank_mask:0xf
	v_exp_f32_e32 v138, v121
	v_cndmask_b32_e64 v118, v118, 4, s[76:77]
	v_mfma_f32_16x16x4_f32 v[42:45], v255, v3, v[42:45]
	v_sub_f32_e32 v121, v184, v114
	v_cmp_eq_f32_e64 s[74:75], v184, v114
	v_exp_f32_e32 v137, v120
	v_cndmask_b32_e64 v118, v118, 3, s[72:73]
	v_max_f32_dpp v115, v115, v115 row_ror:2 row_mask:0xf bank_mask:0xf
	v_sub_f32_e32 v120, v180, v114
	v_cmp_eq_f32_e64 s[76:77], v180, v114
	v_exp_f32_e32 v136, v121
	v_cndmask_b32_e64 v118, v118, 2, s[74:75]
	v_mfma_f32_16x16x4_f32 v[46:49], v255, v5, v[46:49]
	global_load_dwordx4 v[2:5], v104, s[86:87] offset:1024
	v_sub_f32_e32 v121, v176, v114
	v_max_f32_dpp v115, v115, v115 row_ror:4 row_mask:0xf bank_mask:0xf
	v_cmp_eq_f32_e64 s[72:73], v176, v114
	v_exp_f32_e32 v135, v120
	v_cndmask_b32_e64 v118, v118, 1, s[76:77]
	v_exp_f32_e32 v134, v121
	v_cndmask_b32_e64 v118, v118, 0, s[72:73]
	v_max_f32_dpp v115, v115, v115 row_ror:8 row_mask:0xf bank_mask:0xf
	v_sub_f32_e32 v120, v237, v115
	v_cmp_eq_f32_e64 s[72:73], v237, v115
	v_max3_f32 v114, v178, v182, v186
	s_waitcnt vmcnt(27)
	v_mfma_f32_16x16x4_f32 v[50:53], v254, v10, 0
	v_sub_f32_e32 v121, v233, v115
	v_and_b32_e32 v122, 12, v118
	v_cmp_eq_f32_e64 s[74:75], v233, v115
	v_and_b32_e32 v124, 3, v118
	v_exp_f32_e32 v175, v120
	v_add_f32_e32 v128, v134, v135
	v_cndmask_b32_e64 v119, v155, 15, s[72:73]
	v_add_f32_e32 v130, v136, v137
	v_sub_f32_e32 v120, v229, v115
	v_lshl_or_b32 v122, v122, 4, v124
	v_cmp_eq_f32_e64 s[76:77], v229, v115
	v_max3_f32 v116, v190, v194, v198
	v_exp_f32_e32 v174, v121
	v_add_f32_e32 v128, v128, v138
	v_cndmask_b32_e64 v119, v119, 14, s[74:75]
	v_add_f32_e32 v130, v130, v139
	v_mfma_f32_16x16x4_f32 v[54:57], v254, v12, 0
	v_sub_f32_e32 v121, v225, v115
	v_or_b32_e32 v122, v122, v102
	v_cmp_eq_f32_e64 s[72:73], v225, v115
	v_add_f32_e32 v128, v128, v140
	v_exp_f32_e32 v173, v120
	v_max3_f32 v114, v114, v202, v206
	v_cndmask_b32_e64 v119, v119, 13, s[76:77]
	v_add_f32_e32 v130, v130, v141
	v_sub_f32_e32 v120, v221, v115
	v_max_u32_e32 v126, v122, v118
	v_cmp_eq_f32_e64 s[74:75], v221, v115
	v_add_f32_e32 v128, v128, v142
	v_exp_f32_e32 v172, v121
	v_add_f32_e32 v130, v130, v143
	v_cndmask_b32_e64 v119, v119, 12, s[72:73]
	v_max3_f32 v116, v116, v210, v214
	v_mfma_f32_16x16x4_f32 v[50:53], v255, v11, v[50:53]
	v_sub_f32_e32 v121, v217, v115
	v_min_u32_dpp v126, v126, v126 row_ror:1 row_mask:0xf bank_mask:0xf
	v_cmp_eq_f32_e64 s[76:77], v217, v115
	v_add_f32_e32 v128, v128, v144
	v_exp_f32_e32 v171, v120
	v_add_f32_e32 v130, v130, v145
	v_cndmask_b32_e64 v119, v119, 11, s[74:75]
	v_min_u32_dpp v126, v126, v126 row_ror:2 row_mask:0xf bank_mask:0xf
	v_sub_f32_e32 v120, v213, v115
	v_max3_f32 v114, v114, v218, v222
	v_cmp_eq_f32_e64 s[72:73], v213, v115
	v_add_f32_e32 v128, v128, v146
	v_exp_f32_e32 v170, v121
	v_add_f32_e32 v130, v130, v147
	v_cndmask_b32_e64 v119, v119, 10, s[76:77]
	v_min_u32_dpp v126, v126, v126 row_ror:4 row_mask:0xf bank_mask:0xf
	v_mfma_f32_16x16x4_f32 v[54:57], v255, v13, v[54:57]
	global_load_dwordx4 v[10:13], v104, s[86:87] offset:2048
	v_sub_f32_e32 v121, v209, v115
	v_add_f32_e32 v128, v128, v148
	v_cmp_eq_f32_e64 s[74:75], v209, v115
	v_add_f32_e32 v130, v130, v149
	v_exp_f32_e32 v169, v120
	v_max3_f32 v116, v116, v226, v230
	v_cndmask_b32_e64 v119, v119, 9, s[72:73]
	v_min_u32_dpp v126, v126, v126 row_ror:8 row_mask:0xf bank_mask:0xf
	v_sub_f32_e32 v120, v205, v115
	v_add_f32_e32 v128, v128, v130
	v_cmp_eq_f32_e64 s[76:77], v205, v115
	v_mad_u32_u24 v248, v126, 24, v107
	v_exp_f32_e32 v168, v121
	v_add_f32_dpp v128, v128, v128 row_ror:1 row_mask:0xf bank_mask:0xf
	v_cndmask_b32_e64 v119, v119, 8, s[74:75]
	v_max3_f32 v114, v114, v234, v238
	s_waitcnt vmcnt(23)
	v_mfma_f32_16x16x4_f32 v[58:61], v254, v14, 0
	v_sub_f32_e32 v121, v201, v115
	global_load_dword v159, v248, s[92:93]
	v_cmp_eq_f32_e64 s[72:73], v201, v115
	v_add_f32_dpp v128, v128, v128 row_ror:2 row_mask:0xf bank_mask:0xf
	v_exp_f32_e32 v167, v120
	s_nop 0
	v_add_f32_dpp v128, v128, v128 row_ror:4 row_mask:0xf bank_mask:0xf
	v_cndmask_b32_e64 v119, v119, 7, s[76:77]
	s_nop 0
	v_add_f32_dpp v128, v128, v128 row_ror:8 row_mask:0xf bank_mask:0xf
	v_sub_f32_e32 v120, v197, v115
	v_max_f32_e32 v114, v114, v116
	v_cmp_eq_f32_e64 s[74:75], v197, v115
	v_rcp_f32_e32 v244, v128
	v_exp_f32_e32 v166, v121
	v_mul_f32_e32 v134, v244, v134
	v_cndmask_b32_e64 v119, v119, 6, s[72:73]
	v_mul_f32_e32 v135, v244, v135
	v_mfma_f32_16x16x4_f32 v[62:65], v254, v16, 0
	v_sub_f32_e32 v121, v193, v115
	v_mul_f32_e32 v136, v244, v136
	v_cmp_eq_f32_e64 s[76:77], v193, v115
	v_max_f32_dpp v114, v114, v114 row_ror:1 row_mask:0xf bank_mask:0xf
	v_exp_f32_e32 v165, v120
	v_mul_f32_e32 v137, v244, v137
	v_cndmask_b32_e64 v119, v119, 5, s[74:75]
	global_store_dwordx4 v108, v[134:137], s[90:91] sc1
	v_sub_f32_e32 v120, v189, v115
	v_mul_f32_e32 v138, v244, v138
	v_cmp_eq_f32_e64 s[72:73], v189, v115
	v_mul_f32_e32 v139, v244, v139
	v_exp_f32_e32 v164, v121
	v_mul_f32_e32 v140, v244, v140
	v_cndmask_b32_e64 v119, v119, 4, s[76:77]
	v_max_f32_dpp v114, v114, v114 row_ror:2 row_mask:0xf bank_mask:0xf
	v_mfma_f32_16x16x4_f32 v[58:61], v255, v15, v[58:61]
	v_sub_f32_e32 v121, v185, v115
	v_mul_f32_e32 v141, v244, v141
	v_cmp_eq_f32_e64 s[74:75], v185, v115
	global_store_dwordx4 v108, v[138:141], s[90:91] offset:256 sc1
	v_exp_f32_e32 v163, v120
	v_mul_f32_e32 v142, v244, v142
	v_cndmask_b32_e64 v119, v119, 3, s[72:73]
	v_mul_f32_e32 v143, v244, v143
	v_sub_f32_e32 v120, v181, v115
	v_max_f32_dpp v114, v114, v114 row_ror:4 row_mask:0xf bank_mask:0xf
	v_cmp_eq_f32_e64 s[76:77], v181, v115
	v_mul_f32_e32 v144, v244, v144
	v_exp_f32_e32 v162, v121
	v_mul_f32_e32 v145, v244, v145
	v_cndmask_b32_e64 v119, v119, 2, s[74:75]
	global_store_dwordx4 v108, v[142:145], s[90:91] offset:512 sc1
	v_mfma_f32_16x16x4_f32 v[62:65], v255, v17, v[62:65]
	global_load_dwordx4 v[14:17], v104, s[86:87] offset:3072
	v_sub_f32_e32 v121, v177, v115
	v_mul_f32_e32 v146, v244, v146
	v_cmp_eq_f32_e64 s[72:73], v177, v115
	v_max_f32_dpp v114, v114, v114 row_ror:8 row_mask:0xf bank_mask:0xf
	v_exp_f32_e32 v161, v120
	v_mul_f32_e32 v147, v244, v147
	v_cndmask_b32_e64 v119, v119, 1, s[76:77]
	v_mul_f32_e32 v148, v244, v148
	v_exp_f32_e32 v160, v121
	v_mul_f32_e32 v149, v244, v149
	v_cndmask_b32_e64 v119, v119, 0, s[72:73]
	global_store_dwordx4 v108, v[146:149], s[90:91] offset:768 sc1
	v_sub_f32_e32 v120, v238, v114
	s_waitcnt vmcnt(13)
	v_cmp_eq_f32_e64 s[72:73], v238, v114
	v_add_u32_e32 v113, s83, v106
	s_waitcnt vmcnt(27)
	v_mfma_f32_16x16x4_f32 v[66:69], v254, v18, 0
	v_sub_f32_e32 v121, v234, v114
	ds_read2st64_b32 v[250:251], v113 offset1:12
	v_cmp_eq_f32_e64 s[74:75], v234, v114
	ds_read2st64_b32 v[252:253], v113 offset0:24 offset1:36
	v_exp_f32_e32 v149, v120
	v_max3_f32 v115, v179, v183, v187
	v_cndmask_b32_e64 v118, v155, 15, s[72:73]
	v_and_b32_e32 v123, 12, v119
	v_sub_f32_e32 v120, v230, v114
	v_and_b32_e32 v125, 3, v119
	v_cmp_eq_f32_e64 s[76:77], v230, v114
	v_add_f32_e32 v129, v160, v161
	v_exp_f32_e32 v148, v121
	v_add_f32_e32 v131, v162, v163
	v_cndmask_b32_e64 v118, v118, 14, s[74:75]
	v_lshl_or_b32 v123, v123, 4, v125
	v_mfma_f32_16x16x4_f32 v[70:73], v254, v20, 0
	v_sub_f32_e32 v121, v226, v114
	v_max3_f32 v117, v191, v195, v199
	v_cmp_eq_f32_e64 s[72:73], v226, v114
	v_add_f32_e32 v129, v129, v164
	v_exp_f32_e32 v147, v120
	v_add_f32_e32 v131, v131, v165
	v_cndmask_b32_e64 v118, v118, 13, s[76:77]
	v_or_b32_e32 v123, v123, v102
	v_sub_f32_e32 v120, v222, v114
	v_add_f32_e32 v129, v129, v166
	v_cmp_eq_f32_e64 s[74:75], v222, v114
	v_max3_f32 v115, v115, v203, v207
	v_exp_f32_e32 v146, v121
	v_add_f32_e32 v131, v131, v167
	v_cndmask_b32_e64 v118, v118, 12, s[72:73]
	v_max_u32_e32 v127, v123, v119
	v_mfma_f32_16x16x4_f32 v[66:69], v255, v19, v[66:69]
	v_sub_f32_e32 v121, v218, v114
	v_add_f32_e32 v129, v129, v168
	v_cmp_eq_f32_e64 s[76:77], v218, v114
	v_add_f32_e32 v131, v131, v169
	v_exp_f32_e32 v145, v120
	v_max3_f32 v117, v117, v211, v215
	v_cndmask_b32_e64 v118, v118, 11, s[74:75]
	v_min_u32_dpp v127, v127, v127 row_ror:1 row_mask:0xf bank_mask:0xf
	v_add_f32_e32 v129, v129, v170
	v_sub_f32_e32 v120, v214, v114
	v_add_f32_e32 v131, v131, v171
	v_cmp_eq_f32_e64 s[72:73], v214, v114
	v_min_u32_dpp v127, v127, v127 row_ror:2 row_mask:0xf bank_mask:0xf
	v_exp_f32_e32 v144, v121
	v_max3_f32 v115, v115, v219, v223
	v_cndmask_b32_e64 v118, v118, 10, s[76:77]
	v_add_f32_e32 v129, v129, v172
	v_mfma_f32_16x16x4_f32 v[70:73], v255, v21, v[70:73]
	global_load_dwordx4 v[18:21], v104, s[88:89]
	v_sub_f32_e32 v121, v210, v114
	v_add_f32_e32 v131, v131, v173
	v_cmp_eq_f32_e64 s[74:75], v210, v114
	v_min_u32_dpp v127, v127, v127 row_ror:4 row_mask:0xf bank_mask:0xf
	v_exp_f32_e32 v143, v120
	v_add_f32_e32 v129, v129, v174
	v_cndmask_b32_e64 v118, v118, 9, s[72:73]
	v_add_f32_e32 v131, v131, v175
	v_sub_f32_e32 v120, v206, v114
	v_max3_f32 v117, v117, v227, v231
	v_cmp_eq_f32_e64 s[76:77], v206, v114
	v_min_u32_dpp v127, v127, v127 row_ror:8 row_mask:0xf bank_mask:0xf
	v_exp_f32_e32 v142, v121
	v_add_f32_e32 v129, v129, v131
	v_cndmask_b32_e64 v118, v118, 8, s[74:75]
	v_mad_u32_u24 v249, v127, 24, v107
	s_waitcnt vmcnt(24)
	v_mfma_f32_16x16x4_f32 v[74:77], v254, v22, 0
	v_sub_f32_e32 v121, v202, v114
	v_add_f32_dpp v129, v129, v129 row_ror:1 row_mask:0xf bank_mask:0xf
	v_cmp_eq_f32_e64 s[72:73], v202, v114
	v_max3_f32 v115, v115, v235, v239
	v_exp_f32_e32 v141, v120
	global_load_dword v158, v249, s[92:93]
	v_cndmask_b32_e64 v118, v118, 7, s[76:77]
	v_add_f32_dpp v129, v129, v129 row_ror:2 row_mask:0xf bank_mask:0xf
	v_sub_f32_e32 v120, v198, v114
	s_nop 0
	v_add_f32_dpp v129, v129, v129 row_ror:4 row_mask:0xf bank_mask:0xf
	v_cmp_eq_f32_e64 s[74:75], v198, v114
	s_nop 0
	v_add_f32_dpp v129, v129, v129 row_ror:8 row_mask:0xf bank_mask:0xf
	v_exp_f32_e32 v140, v121
	v_max_f32_e32 v115, v115, v117
	v_cndmask_b32_e64 v118, v118, 6, s[72:73]
	v_rcp_f32_e32 v246, v129
	v_mfma_f32_16x16x4_f32 v[78:81], v254, v24, 0
	v_sub_f32_e32 v121, v194, v114
	v_mul_f32_e32 v160, v246, v160
	v_mul_f32_e32 v161, v246, v161
	v_cmp_eq_f32_e64 s[76:77], v194, v114
	v_mul_f32_e32 v162, v246, v162
	v_exp_f32_e32 v139, v120
	v_max_f32_dpp v115, v115, v115 row_ror:1 row_mask:0xf bank_mask:0xf
	v_cndmask_b32_e64 v118, v118, 5, s[74:75]
	v_mul_f32_e32 v163, v246, v163
	v_sub_f32_e32 v120, v190, v114
	global_store_dwordx4 v109, v[160:163], s[90:91] sc1
	v_cmp_eq_f32_e64 s[72:73], v190, v114
	v_mul_f32_e32 v164, v246, v164
	v_exp_f32_e32 v138, v121
	v_mul_f32_e32 v165, v246, v165
	v_cndmask_b32_e64 v118, v118, 4, s[76:77]
	v_mul_f32_e32 v166, v246, v166
	v_mfma_f32_16x16x4_f32 v[74:77], v255, v23, v[74:77]
	v_sub_f32_e32 v121, v186, v114
	v_max_f32_dpp v115, v115, v115 row_ror:2 row_mask:0xf bank_mask:0xf
	v_cmp_eq_f32_e64 s[74:75], v186, v114
	v_mul_f32_e32 v167, v246, v167
	v_exp_f32_e32 v137, v120
	global_store_dwordx4 v109, v[164:167], s[90:91] offset:256 sc1
	v_cndmask_b32_e64 v118, v118, 3, s[72:73]
	v_mul_f32_e32 v168, v246, v168
	v_sub_f32_e32 v120, v182, v114
	v_mul_f32_e32 v169, v246, v169
	v_cmp_eq_f32_e64 s[76:77], v182, v114
	v_max_f32_dpp v115, v115, v115 row_ror:4 row_mask:0xf bank_mask:0xf
	v_exp_f32_e32 v136, v121
	v_mul_f32_e32 v170, v246, v170
	v_cndmask_b32_e64 v118, v118, 2, s[74:75]
	v_mul_f32_e32 v171, v246, v171
	v_mfma_f32_16x16x4_f32 v[78:81], v255, v25, v[78:81]
	global_load_dwordx4 v[22:25], v104, s[88:89] offset:1024
	v_sub_f32_e32 v121, v178, v114
	global_store_dwordx4 v109, v[168:171], s[90:91] offset:512 sc1
	v_cmp_eq_f32_e64 s[72:73], v178, v114
	v_mul_f32_e32 v172, v246, v172
	v_exp_f32_e32 v135, v120
	v_max_f32_dpp v115, v115, v115 row_ror:8 row_mask:0xf bank_mask:0xf
	v_cndmask_b32_e64 v118, v118, 1, s[76:77]
	v_mul_f32_e32 v173, v246, v173
	v_exp_f32_e32 v134, v121
	v_mul_f32_e32 v174, v246, v174
	v_cndmask_b32_e64 v118, v118, 0, s[72:73]
	v_mul_f32_e32 v175, v246, v175
	global_store_dwordx4 v109, v[172:175], s[90:91] offset:768 sc1
	v_sub_f32_e32 v120, v239, v115
	v_cmp_eq_f32_e64 s[72:73], v239, v115
	s_waitcnt lgkmcnt(0)
	s_waitcnt vmcnt(27)
	v_mfma_f32_16x16x4_f32 v[82:85], v254, v26, 0
	v_sub_f32_e32 v121, v235, v115
	v_add_f32_e32 v250, v240, v250
	v_cmp_eq_f32_e64 s[74:75], v235, v115
	v_add_f32_e32 v251, v241, v251
	v_exp_f32_e32 v175, v120
	v_add_f32_e32 v252, v242, v252
	v_cndmask_b32_e64 v119, v155, 15, s[72:73]
	v_add_f32_e32 v253, v243, v253
	v_sub_f32_e32 v120, v231, v115
	ds_write2st64_b32 v113, v250, v251 offset1:12
	v_cmp_eq_f32_e64 s[76:77], v231, v115
	ds_write2st64_b32 v113, v252, v253 offset0:24 offset1:36
	v_exp_f32_e32 v174, v121
	v_and_b32_e32 v122, 12, v118
	v_cndmask_b32_e64 v119, v119, 14, s[74:75]
	v_and_b32_e32 v124, 3, v118
	v_mfma_f32_16x16x4_f32 v[86:89], v254, v28, 0
	v_sub_f32_e32 v121, v227, v115
	v_cmp_eq_f32_e64 s[72:73], v227, v115
	v_add_f32_e32 v128, v134, v135
	v_exp_f32_e32 v173, v120
	v_add_f32_e32 v130, v136, v137
	v_cndmask_b32_e64 v119, v119, 13, s[76:77]
	v_lshl_or_b32 v122, v122, 4, v124
	v_sub_f32_e32 v120, v223, v115
	v_add_f32_e32 v128, v128, v138
	v_cmp_eq_f32_e64 s[74:75], v223, v115
	v_add_f32_e32 v130, v130, v139
	v_exp_f32_e32 v172, v121
	v_or_b32_e32 v122, v122, v102
	v_cndmask_b32_e64 v119, v119, 12, s[72:73]
	v_add_f32_e32 v128, v128, v140
	v_mfma_f32_16x16x4_f32 v[82:85], v255, v27, v[82:85]
	v_sub_f32_e32 v121, v219, v115
	v_add_f32_e32 v130, v130, v141
	v_cmp_eq_f32_e64 s[76:77], v219, v115
	v_max_u32_e32 v126, v122, v118
	v_exp_f32_e32 v171, v120
	v_add_f32_e32 v128, v128, v142
	v_cndmask_b32_e64 v119, v119, 11, s[74:75]
	v_sub_f32_e32 v120, v215, v115
	v_add_f32_e32 v130, v130, v143
	v_cmp_eq_f32_e64 s[72:73], v215, v115
	v_min_u32_dpp v126, v126, v126 row_ror:1 row_mask:0xf bank_mask:0xf
	v_exp_f32_e32 v170, v121
	v_add_f32_e32 v128, v128, v144
	v_cndmask_b32_e64 v119, v119, 10, s[76:77]
	v_add_f32_e32 v130, v130, v145
	v_mfma_f32_16x16x4_f32 v[86:89], v255, v29, v[86:89]
	global_load_dwordx4 v[26:29], v104, s[88:89] offset:2048
	v_sub_f32_e32 v121, v211, v115
	v_min_u32_dpp v126, v126, v126 row_ror:2 row_mask:0xf bank_mask:0xf
	v_cmp_eq_f32_e64 s[74:75], v211, v115
	v_add_f32_e32 v128, v128, v146
	v_exp_f32_e32 v169, v120
	v_add_f32_e32 v130, v130, v147
	v_cndmask_b32_e64 v119, v119, 9, s[72:73]
	v_min_u32_dpp v126, v126, v126 row_ror:4 row_mask:0xf bank_mask:0xf
	v_sub_f32_e32 v120, v207, v115
	v_add_f32_e32 v128, v128, v148
	v_cmp_eq_f32_e64 s[76:77], v207, v115
	v_add_f32_e32 v130, v130, v149
	v_exp_f32_e32 v168, v121
	v_cndmask_b32_e64 v119, v119, 8, s[74:75]
	v_min_u32_dpp v126, v126, v126 row_ror:8 row_mask:0xf bank_mask:0xf
	s_waitcnt vmcnt(24)
	v_mfma_f32_16x16x4_f32 v[90:93], v254, v30, 0
	v_sub_f32_e32 v121, v203, v115
	v_add_f32_e32 v128, v128, v130
	v_cmp_eq_f32_e64 s[72:73], v203, v115
	v_mad_u32_u24 v248, v126, 24, v107
	v_exp_f32_e32 v167, v120
	v_add_f32_dpp v128, v128, v128 row_ror:1 row_mask:0xf bank_mask:0xf
	v_cndmask_b32_e64 v119, v119, 7, s[76:77]
	global_load_dword v157, v248, s[92:93]
	v_sub_f32_e32 v120, v199, v115
	v_add_f32_dpp v128, v128, v128 row_ror:2 row_mask:0xf bank_mask:0xf
	v_cmp_eq_f32_e64 s[74:75], v199, v115
	s_nop 0
	v_add_f32_dpp v128, v128, v128 row_ror:4 row_mask:0xf bank_mask:0xf
	v_exp_f32_e32 v166, v121
	s_nop 0
	v_add_f32_dpp v128, v128, v128 row_ror:8 row_mask:0xf bank_mask:0xf
	v_cndmask_b32_e64 v119, v119, 6, s[72:73]
	v_rcp_f32_e32 v244, v128
	v_mfma_f32_16x16x4_f32 v[94:97], v254, v32, 0
	v_sub_f32_e32 v121, v195, v115
	v_cmp_eq_f32_e64 s[76:77], v195, v115
	v_mul_f32_e32 v134, v244, v134
	v_exp_f32_e32 v165, v120
	v_mul_f32_e32 v135, v244, v135
	v_cndmask_b32_e64 v119, v119, 5, s[74:75]
	v_mul_f32_e32 v136, v244, v136
	v_sub_f32_e32 v120, v191, v115
	v_mul_f32_e32 v137, v244, v137
	v_cmp_eq_f32_e64 s[72:73], v191, v115
	global_store_dwordx4 v110, v[134:137], s[90:91] sc1
	v_exp_f32_e32 v164, v121
	v_mul_f32_e32 v138, v244, v138
	v_cndmask_b32_e64 v119, v119, 4, s[76:77]
	v_mul_f32_e32 v139, v244, v139
	v_mfma_f32_16x16x4_f32 v[90:93], v255, v31, v[90:93]
	v_sub_f32_e32 v121, v187, v115
	v_mul_f32_e32 v140, v244, v140
	v_cmp_eq_f32_e64 s[74:75], v187, v115
	v_mul_f32_e32 v141, v244, v141
	v_exp_f32_e32 v163, v120
	global_store_dwordx4 v110, v[138:141], s[90:91] offset:256 sc1
	v_cndmask_b32_e64 v119, v119, 3, s[72:73]
	v_sub_f32_e32 v120, v183, v115
	v_mul_f32_e32 v142, v244, v142
	v_cmp_eq_f32_e64 s[76:77], v183, v115
	v_mul_f32_e32 v143, v244, v143
	v_exp_f32_e32 v162, v121
	v_mul_f32_e32 v144, v244, v144
	v_cndmask_b32_e64 v119, v119, 2, s[74:75]
	v_mul_f32_e32 v145, v244, v145
	v_mfma_f32_16x16x4_f32 v[94:97], v255, v33, v[94:97]
	global_load_dwordx4 v[30:33], v104, s[88:89] offset:3072
	v_sub_f32_e32 v121, v179, v115
	global_store_dwordx4 v110, v[142:145], s[90:91] offset:512 sc1
	v_cmp_eq_f32_e64 s[72:73], v179, v115
	v_mul_f32_e32 v146, v244, v146
	v_exp_f32_e32 v161, v120
	v_mul_f32_e32 v147, v244, v147
	v_cndmask_b32_e64 v119, v119, 1, s[76:77]
	v_mul_f32_e32 v148, v244, v148
	v_exp_f32_e32 v160, v121
	v_mul_f32_e32 v149, v244, v149
	v_cndmask_b32_e64 v119, v119, 0, s[72:73]
	global_store_dwordx4 v110, v[146:149], s[90:91] offset:768 sc1
	v_and_b32_e32 v123, 12, v119
	v_max3_f32 v114, v34, v38, v42
	v_and_b32_e32 v125, 3, v119
	v_add_f32_e32 v129, v160, v161
	v_add_f32_e32 v131, v162, v163
	v_lshl_or_b32 v123, v123, 4, v125
	v_max3_f32 v116, v46, v50, v54
	v_add_f32_e32 v129, v129, v164
	v_add_f32_e32 v131, v131, v165
	v_or_b32_e32 v123, v123, v102
	v_add_f32_e32 v129, v129, v166
	v_max3_f32 v114, v114, v58, v62
	v_add_f32_e32 v131, v131, v167
	v_max_u32_e32 v127, v123, v119
	v_add_f32_e32 v129, v129, v168
	v_add_f32_e32 v131, v131, v169
	v_max3_f32 v116, v116, v66, v70
	v_min_u32_dpp v127, v127, v127 row_ror:1 row_mask:0xf bank_mask:0xf
	v_add_f32_e32 v129, v129, v170
	v_add_f32_e32 v131, v131, v171
	v_min_u32_dpp v127, v127, v127 row_ror:2 row_mask:0xf bank_mask:0xf
	v_add_f32_e32 v129, v129, v172
	v_max3_f32 v114, v114, v74, v78
	v_add_f32_e32 v131, v131, v173
	v_min_u32_dpp v127, v127, v127 row_ror:4 row_mask:0xf bank_mask:0xf
	v_add_f32_e32 v129, v129, v174
	v_add_f32_e32 v131, v131, v175
	v_max3_f32 v116, v116, v82, v86
	v_min_u32_dpp v127, v127, v127 row_ror:8 row_mask:0xf bank_mask:0xf
	v_add_f32_e32 v129, v129, v131
	v_mad_u32_u24 v249, v127, 24, v107
	s_nop 0
	v_add_f32_dpp v129, v129, v129 row_ror:1 row_mask:0xf bank_mask:0xf
	v_max3_f32 v114, v114, v90, v94
	global_load_dword v156, v249, s[92:93]
	v_add_f32_dpp v129, v129, v129 row_ror:2 row_mask:0xf bank_mask:0xf
	s_nop 1
	v_add_f32_dpp v129, v129, v129 row_ror:4 row_mask:0xf bank_mask:0xf
	s_nop 1
	v_add_f32_dpp v129, v129, v129 row_ror:8 row_mask:0xf bank_mask:0xf
	v_max_f32_e32 v114, v114, v116
	v_rcp_f32_e32 v246, v129
	s_nop 0
	v_mul_f32_e32 v160, v246, v160
	v_mul_f32_e32 v161, v246, v161
	v_mul_f32_e32 v162, v246, v162
	v_mul_f32_e32 v163, v246, v163
	v_max_f32_dpp v114, v114, v114 row_ror:1 row_mask:0xf bank_mask:0xf
	global_store_dwordx4 v111, v[160:163], s[90:91] sc1
	v_mul_f32_e32 v164, v246, v164
	v_mul_f32_e32 v165, v246, v165
	v_mul_f32_e32 v166, v246, v166
	v_max_f32_dpp v114, v114, v114 row_ror:2 row_mask:0xf bank_mask:0xf
	v_mul_f32_e32 v167, v246, v167
	global_store_dwordx4 v111, v[164:167], s[90:91] offset:256 sc1
	v_mul_f32_e32 v168, v246, v168
	v_mul_f32_e32 v169, v246, v169
	v_max_f32_dpp v114, v114, v114 row_ror:4 row_mask:0xf bank_mask:0xf
	v_mul_f32_e32 v170, v246, v170
	v_mul_f32_e32 v171, v246, v171
	global_store_dwordx4 v111, v[168:171], s[90:91] offset:512 sc1
	v_mul_f32_e32 v172, v246, v172
	v_max_f32_dpp v114, v114, v114 row_ror:8 row_mask:0xf bank_mask:0xf
	v_mul_f32_e32 v173, v246, v173
	v_mul_f32_e32 v174, v246, v174
	v_mul_f32_e32 v175, v246, v175
	global_store_dwordx4 v111, v[172:175], s[90:91] offset:768 sc1
	s_add_i32 s70, s70, 1
	s_cmp_lt_u32 s70, 16
	s_cbranch_scc1 .Lk3m_loop
